# three conversion items per wave (was one) for the workgroups idle in the second round of the up-projection GEMM
# speedup vs baseline: 1.0107x; 1.0107x over previous
.Lcvt_t3:
	s_cmp_eq_u32 s31, 3
	s_cbranch_scc0 .Lcvt_t10
	s_sub_i32 s27, s63, 208
	s_cmp_lt_i32 s27, 0
	s_cbranch_scc1 .Lcvt_ret
	s_mov_b32 s26, 3
	s_movk_i32 s30, 5040
	s_movk_i32 s4, 6048
	s_mov_b32 s24, s62
	s_branch .Lcvt_go
.Lcvt_t10:
	s_cmp_eq_u32 s31, 10
	s_cbranch_scc0 .Lcvt_lock
	s_cmp_ge_u32 s62, 3
	s_cbranch_scc1 .Lcvt_ret
	s_sub_i32 s27, s63, 136
	s_cmp_lt_i32 s27, 0
	s_cbranch_scc1 .Lcvt_ret
	s_mov_b32 s26, 4
	s_movk_i32 s30, 6048
	s_movk_i32 s4, 9408
	s_add_i32 s24, s62, 1

.Lcvt_lk_c:
	s_mov_b32 s26, 2647
	s_mov_b32 s4, 18528
	s_cmp_eq_u32 s27, 1
	s_cselect_b32 s26, 1896, s26
	s_cselect_b32 s4, 15168, s4
	s_cmp_eq_u32 s27, 2
	s_cselect_b32 s26, 1896, s26
	s_cselect_b32 s4, 15168, s4
	s_cmp_eq_u32 s27, 3
	s_cselect_b32 s26, 2526, s26
	s_cselect_b32 s4, 20208, s4
	s_mul_i32 s30, s24, s26
	s_add_i32 s24, s30, s26
	s_min_u32 s4, s4, s24
	s_mul_i32 s26, s80, 7
	s_add_i32 s26, s26, s25
	s_add_i32 s26, s26, -1
	s_add_i32 s30, s30, s26
	s_mov_b32 s26, 2
	s_movk_i32 s25, 0x700
.Lcvt_item:
	s_cmp_ge_u32 s30, s4
	s_cbranch_scc1 .Lcvt_ret
	s_mov_b32 s6, s27
	s_mov_b32 s5, s30
	s_cmp_eq_u32 s25, 1
	s_cbranch_scc1 .Lcvt_dec
	s_cmp_eq_u32 s27, 3
	s_cbranch_scc1 .Lcvt_m3
	s_mov_b32 s24, 6048
	s_cmp_eq_u32 s27, 0
	s_cselect_b32 s24, s24, 9408
	s_add_i32 s5, s5, s24
	s_branch .Lcvt_dec
.Lcvt_m3:
	s_cmp_lt_u32 s5, 5040
	s_cbranch_scc1 .Lcvt_dec
	s_add_i32 s5, s5, 4368
